# v10 + GEMM K-loop headers aligned to 256 bytes
# speedup vs baseline: 1.0027x; 1.0015x over previous
;     ...
;         const bool has_next = S.next(ui + 1, nxt);
;         const char* nA = has_next ? (const char*)g.A + (size_t)nxt.pm * tstepA : cA; const char* nB = has_next ? (const char*)g.Bt + (size_t)nxt.pn * tstepB : cB;
;         for (int t = 0; t < nt; t += 2) {
;             const bool last = (t == nt - 2);
;             const char* a1 = cA + (size_t)(t + 1) * kstep;
;             const char* a2 = last ? nA : cA + (size_t)(t + 2) * kstep; const char* b2 = last ? nB : cB + (size_t)(t + 2) * kstep;
;             const char* a3 = a2 + kstep; const char* b3 = b2 + kstep;
;     ...
;         for (int a = 0; a < 2; ++a)
; #pragma unroll
;             for (int b = 0; b < 2; ++b)
; #pragma unroll
;                 for (int m = 0; m < 4; ++m)
; #pragma unroll
;                     for (int n = 0; n < 2; ++n) acc[a][b][m][n] = (f32x4){0.f, 0.f, 0.f, 0.f};
.LBB0_459:
	s_ashr_i32 s23, s22, 31
	s_lshl_b64 s[28:29], s[22:23], 21
	v_readlane_b32 s2, v248, 8
	v_readlane_b32 s3, v248, 9
	s_add_u32 s28, s2, s28
	s_addc_u32 s29, s3, s29
	s_and_b64 s[30:31], s[26:27], exec
	s_cselect_b32 s23, s29, s39
	s_cselect_b32 s35, s28, s38
	s_ashr_i32 s25, s24, 31
	s_lshl_b64 s[30:31], s[24:25], 21
	v_readlane_b32 s2, v249, 48
	s_add_u32 s30, s2, s30
	v_readlane_b32 s2, v249, 49
	s_addc_u32 s31, s2, s31
	s_and_b64 s[42:43], s[26:27], exec
	s_cselect_b32 s25, s31, s41
	s_cselect_b32 s50, s30, s40
	s_add_u32 s51, s40, 0x100
	v_mov_b32_e32 v2, 0
	s_addc_u32 s52, s41, 0
	s_mov_b32 s53, -2
	v_mov_b32_e32 v3, v2
	v_mov_b32_e32 v4, v2
	v_mov_b32_e32 v5, v2
	v_mov_b32_e32 v6, v2
	v_mov_b32_e32 v7, v2
	v_mov_b32_e32 v8, v2
	v_mov_b32_e32 v9, v2
	v_mov_b32_e32 v18, v2
	v_mov_b32_e32 v19, v2
	v_mov_b32_e32 v20, v2
	v_mov_b32_e32 v21, v2
	v_mov_b32_e32 v22, v2
	v_mov_b32_e32 v23, v2
	v_mov_b32_e32 v24, v2
	v_mov_b32_e32 v25, v2
	v_mov_b32_e32 v34, v2
	v_mov_b32_e32 v35, v2
	v_mov_b32_e32 v36, v2
	v_mov_b32_e32 v37, v2
	v_mov_b32_e32 v38, v2
	v_mov_b32_e32 v39, v2
	v_mov_b32_e32 v40, v2
	v_mov_b32_e32 v41, v2
	v_mov_b32_e32 v50, v2
	v_mov_b32_e32 v51, v2
	v_mov_b32_e32 v52, v2
	v_mov_b32_e32 v53, v2
	v_mov_b32_e32 v54, v2
	v_mov_b32_e32 v55, v2
	v_mov_b32_e32 v56, v2
	v_mov_b32_e32 v57, v2
	v_mov_b32_e32 v10, v2
	v_mov_b32_e32 v11, v2
	v_mov_b32_e32 v12, v2
	v_mov_b32_e32 v13, v2
	v_mov_b32_e32 v14, v2
	v_mov_b32_e32 v15, v2
	v_mov_b32_e32 v16, v2
	v_mov_b32_e32 v17, v2
	v_mov_b32_e32 v26, v2
	v_mov_b32_e32 v27, v2
	v_mov_b32_e32 v28, v2
	v_mov_b32_e32 v29, v2
	v_mov_b32_e32 v30, v2
	v_mov_b32_e32 v31, v2
	v_mov_b32_e32 v32, v2
	v_mov_b32_e32 v33, v2
	v_mov_b32_e32 v42, v2
	v_mov_b32_e32 v43, v2
	v_mov_b32_e32 v44, v2
	v_mov_b32_e32 v45, v2
	v_mov_b32_e32 v46, v2
	v_mov_b32_e32 v47, v2
	v_mov_b32_e32 v48, v2
	v_mov_b32_e32 v49, v2
	v_mov_b32_e32 v58, v2
	v_mov_b32_e32 v59, v2
	v_mov_b32_e32 v60, v2
	v_mov_b32_e32 v61, v2
	v_mov_b32_e32 v62, v2
	v_mov_b32_e32 v63, v2
	v_mov_b32_e32 v64, v2
	v_mov_b32_e32 v65, v2
	v_mov_b32_e32 v66, v2
	v_mov_b32_e32 v67, v2
	v_mov_b32_e32 v68, v2
	v_mov_b32_e32 v69, v2
	v_mov_b32_e32 v70, v2
	v_mov_b32_e32 v71, v2
	v_mov_b32_e32 v72, v2
	v_mov_b32_e32 v73, v2
	v_mov_b32_e32 v82, v2
	v_mov_b32_e32 v83, v2
	v_mov_b32_e32 v84, v2
	v_mov_b32_e32 v85, v2
	v_mov_b32_e32 v86, v2
	v_mov_b32_e32 v87, v2
	v_mov_b32_e32 v88, v2
	v_mov_b32_e32 v89, v2
	v_mov_b32_e32 v98, v2
	v_mov_b32_e32 v99, v2
	v_mov_b32_e32 v100, v2
	v_mov_b32_e32 v101, v2
	v_mov_b32_e32 v102, v2
	v_mov_b32_e32 v103, v2
	v_mov_b32_e32 v104, v2
	v_mov_b32_e32 v105, v2
	v_mov_b32_e32 v114, v2
	v_mov_b32_e32 v115, v2
	v_mov_b32_e32 v116, v2
	v_mov_b32_e32 v117, v2
	v_mov_b32_e32 v118, v2
	v_mov_b32_e32 v119, v2
	v_mov_b32_e32 v120, v2
	v_mov_b32_e32 v121, v2
	v_mov_b32_e32 v74, v2
	v_mov_b32_e32 v75, v2
	v_mov_b32_e32 v76, v2
	v_mov_b32_e32 v77, v2
	v_mov_b32_e32 v78, v2
	v_mov_b32_e32 v79, v2
	v_mov_b32_e32 v80, v2
	v_mov_b32_e32 v81, v2
	v_mov_b32_e32 v90, v2
	v_mov_b32_e32 v91, v2
	v_mov_b32_e32 v92, v2
	v_mov_b32_e32 v93, v2
	v_mov_b32_e32 v94, v2
	v_mov_b32_e32 v95, v2
	v_mov_b32_e32 v96, v2
	v_mov_b32_e32 v97, v2
	v_mov_b32_e32 v106, v2
	v_mov_b32_e32 v107, v2
	v_mov_b32_e32 v108, v2
	v_mov_b32_e32 v109, v2
	v_mov_b32_e32 v110, v2
	v_mov_b32_e32 v111, v2
	v_mov_b32_e32 v112, v2
	v_mov_b32_e32 v113, v2
	v_mov_b32_e32 v122, v2
	v_mov_b32_e32 v123, v2
	v_mov_b32_e32 v124, v2
	v_mov_b32_e32 v125, v2
	v_mov_b32_e32 v126, v2
	v_mov_b32_e32 v127, v2
	v_mov_b32_e32 v128, v2
	v_mov_b32_e32 v129, v2
	.p2align	8

;     ...
;         const bool has_next = S.next(ui + 1, nxt);
;         const char* nA = has_next ? (const char*)g.A + (size_t)nxt.pm * tstepA : cA; const char* nB = has_next ? (const char*)g.Bt + (size_t)nxt.pn * tstepB : cB;
;         for (int t = 0; t < nt; t += 2) {
;             const bool last = (t == nt - 2);
;             const char* a1 = cA + (size_t)(t + 1) * kstep;
;             const char* a2 = last ? nA : cA + (size_t)(t + 2) * kstep; const char* b2 = last ? nB : cB + (size_t)(t + 2) * kstep;
;             const char* a3 = a2 + kstep; const char* b3 = b2 + kstep;
;     ...
;         for (int a = 0; a < 2; ++a)
; #pragma unroll
;             for (int b = 0; b < 2; ++b)
; #pragma unroll
;                 for (int m = 0; m < 4; ++m)
; #pragma unroll
;                     for (int n = 0; n < 2; ++n) acc[a][b][m][n] = (f32x4){0.f, 0.f, 0.f, 0.f};
.LBB0_592:
	s_ashr_i32 s61, s60, 31
	s_lshl_b64 s[66:67], s[60:61], 20
	v_readlane_b32 s16, v248, 6
	v_readlane_b32 s17, v248, 7
	s_add_u32 s66, s16, s66
	s_addc_u32 s67, s17, s67
	s_and_b64 s[68:69], s[64:65], exec
	s_cselect_b32 s61, s67, s75
	s_cselect_b32 s71, s66, s74
	s_ashr_i32 s63, s62, 31
	s_lshl_b64 s[68:69], s[62:63], 20
	v_readlane_b32 s16, v249, 40
	v_readlane_b32 s17, v249, 41
	s_add_u32 s68, s16, s68
	s_addc_u32 s69, s17, s69
	s_and_b64 s[78:79], s[64:65], exec
	s_cselect_b32 s63, s69, s77
	s_cselect_b32 s95, s68, s76
	s_add_u32 s96, s76, 0x100
	v_mov_b32_e32 v36, 0
	s_addc_u32 s97, s77, 0
	s_mov_b32 vcc_lo, -2
	v_mov_b32_e32 v37, v36
	v_mov_b32_e32 v38, v36
	v_mov_b32_e32 v39, v36
	v_mov_b32_e32 v40, v36
	v_mov_b32_e32 v41, v36
	v_mov_b32_e32 v42, v36
	v_mov_b32_e32 v43, v36
	v_mov_b32_e32 v52, v36
	v_mov_b32_e32 v53, v36
	v_mov_b32_e32 v54, v36
	v_mov_b32_e32 v55, v36
	v_mov_b32_e32 v56, v36
	v_mov_b32_e32 v57, v36
	v_mov_b32_e32 v58, v36
	v_mov_b32_e32 v59, v36
	v_mov_b32_e32 v68, v36
	v_mov_b32_e32 v69, v36
	v_mov_b32_e32 v70, v36
	v_mov_b32_e32 v71, v36
	v_mov_b32_e32 v72, v36
	v_mov_b32_e32 v73, v36
	v_mov_b32_e32 v74, v36
	v_mov_b32_e32 v75, v36
	v_mov_b32_e32 v84, v36
	v_mov_b32_e32 v85, v36
	v_mov_b32_e32 v86, v36
	v_mov_b32_e32 v87, v36
	v_mov_b32_e32 v88, v36
	v_mov_b32_e32 v89, v36
	v_mov_b32_e32 v90, v36
	v_mov_b32_e32 v91, v36
	v_mov_b32_e32 v44, v36
	v_mov_b32_e32 v45, v36
	v_mov_b32_e32 v46, v36
	v_mov_b32_e32 v47, v36
	v_mov_b32_e32 v48, v36
	v_mov_b32_e32 v49, v36
	v_mov_b32_e32 v50, v36
	v_mov_b32_e32 v51, v36
	v_mov_b32_e32 v60, v36
	v_mov_b32_e32 v61, v36
	v_mov_b32_e32 v62, v36
	v_mov_b32_e32 v63, v36
	v_mov_b32_e32 v64, v36
	v_mov_b32_e32 v65, v36
	v_mov_b32_e32 v66, v36
	v_mov_b32_e32 v67, v36
	v_mov_b32_e32 v76, v36
	v_mov_b32_e32 v77, v36
	v_mov_b32_e32 v78, v36
	v_mov_b32_e32 v79, v36
	v_mov_b32_e32 v80, v36
	v_mov_b32_e32 v81, v36
	v_mov_b32_e32 v82, v36
	v_mov_b32_e32 v83, v36
	v_mov_b32_e32 v92, v36
	v_mov_b32_e32 v93, v36
	v_mov_b32_e32 v94, v36
	v_mov_b32_e32 v95, v36
	v_mov_b32_e32 v96, v36
	v_mov_b32_e32 v97, v36
	v_mov_b32_e32 v98, v36
	v_mov_b32_e32 v99, v36
	v_mov_b32_e32 v100, v36
	v_mov_b32_e32 v101, v36
	v_mov_b32_e32 v102, v36
	v_mov_b32_e32 v103, v36
	v_mov_b32_e32 v104, v36
	v_mov_b32_e32 v105, v36
	v_mov_b32_e32 v106, v36
	v_mov_b32_e32 v107, v36
	v_mov_b32_e32 v116, v36
	v_mov_b32_e32 v117, v36
	v_mov_b32_e32 v118, v36
	v_mov_b32_e32 v119, v36
	v_mov_b32_e32 v120, v36
	v_mov_b32_e32 v121, v36
	v_mov_b32_e32 v122, v36
	v_mov_b32_e32 v123, v36
	v_mov_b32_e32 v132, v36
	v_mov_b32_e32 v133, v36
	v_mov_b32_e32 v134, v36
	v_mov_b32_e32 v135, v36
	v_mov_b32_e32 v136, v36
	v_mov_b32_e32 v137, v36
	v_mov_b32_e32 v138, v36
	v_mov_b32_e32 v139, v36
	v_mov_b32_e32 v148, v36
	v_mov_b32_e32 v149, v36
	v_mov_b32_e32 v150, v36
	v_mov_b32_e32 v151, v36
	v_mov_b32_e32 v152, v36
	v_mov_b32_e32 v153, v36
	v_mov_b32_e32 v154, v36
	v_mov_b32_e32 v155, v36
	v_mov_b32_e32 v108, v36
	v_mov_b32_e32 v109, v36
	v_mov_b32_e32 v110, v36
	v_mov_b32_e32 v111, v36
	v_mov_b32_e32 v112, v36
	v_mov_b32_e32 v113, v36
	v_mov_b32_e32 v114, v36
	v_mov_b32_e32 v115, v36
	v_mov_b32_e32 v124, v36
	v_mov_b32_e32 v125, v36
	v_mov_b32_e32 v126, v36
	v_mov_b32_e32 v127, v36
	v_mov_b32_e32 v128, v36
	v_mov_b32_e32 v129, v36
	v_mov_b32_e32 v130, v36
	v_mov_b32_e32 v131, v36
	v_mov_b32_e32 v140, v36
	v_mov_b32_e32 v141, v36
	v_mov_b32_e32 v142, v36
	v_mov_b32_e32 v143, v36
	v_mov_b32_e32 v144, v36
	v_mov_b32_e32 v145, v36
	v_mov_b32_e32 v146, v36
	v_mov_b32_e32 v147, v36
	v_mov_b32_e32 v156, v36
	v_mov_b32_e32 v157, v36
	v_mov_b32_e32 v158, v36
	v_mov_b32_e32 v159, v36
	v_mov_b32_e32 v160, v36
	v_mov_b32_e32 v161, v36
	v_mov_b32_e32 v162, v36
	v_mov_b32_e32 v163, v36
	.p2align	8

;     ...
;         const bool has_next = S.next(ui + 1, nxt);
;         const char* nA = has_next ? (const char*)g.A + (size_t)nxt.pm * tstepA : cA; const char* nB = has_next ? (const char*)g.Bt + (size_t)nxt.pn * tstepB : cB;
;         for (int t = 0; t < nt; t += 2) {
;             const bool last = (t == nt - 2);
;             const char* a1 = cA + (size_t)(t + 1) * kstep;
;             const char* a2 = last ? nA : cA + (size_t)(t + 2) * kstep; const char* b2 = last ? nB : cB + (size_t)(t + 2) * kstep;
;             const char* a3 = a2 + kstep; const char* b3 = b2 + kstep;
;     ...
;         for (int a = 0; a < 2; ++a)
; #pragma unroll
;             for (int b = 0; b < 2; ++b)
; #pragma unroll
;                 for (int m = 0; m < 4; ++m)
; #pragma unroll
;                     for (int n = 0; n < 2; ++n) acc[a][b][m][n] = (f32x4){0.f, 0.f, 0.f, 0.f};
;     __device__ __forceinline__ void mid(f32x4 (&acc)[2][2][4][2], const Unit& u, int wr, int wc, int fr, int fq) const {
;         const bf16* pb = P + (size_t)(u.pm * 256 + wr * 64 + fr) * PNP + (u.pn * 256 + wc * 32 + 8 * fq);
;         asm volatile("" : "+v"(pb));
.LBB0_1707:
	s_ashr_i32 s23, s22, 31
	s_lshl_b64 s[24:25], s[22:23], 20
	s_add_u32 s24, s68, s24
	s_addc_u32 s25, s69, s25
	s_and_b64 s[26:27], s[2:3], exec
	s_cselect_b32 s23, s25, s29
	s_cselect_b32 s52, s24, s28
	s_ashr_i32 s21, s20, 31
	s_lshl_b64 s[26:27], s[20:21], 20
	v_readlane_b32 s36, v249, 50
	v_readlane_b32 s37, v249, 51
	s_add_u32 s26, s36, s26
	s_addc_u32 s27, s37, s27
	s_and_b64 s[36:37], s[2:3], exec
	v_lshl_add_u32 v200, s34, 8, v1
	v_lshl_or_b32 v202, s35, 8, v183
	s_mov_b32 s34, 0x8a00
	v_mov_b32_e32 v28, v26
	v_mov_b32_e32 v29, v26
	s_cselect_b32 s21, s27, s31
	s_cselect_b32 s53, s26, s30
	v_ashrrev_i32_e32 v203, 31, v202
	v_mad_i64_i32 v[2:3], s[34:35], v200, s34, v[198:199]
	s_add_u32 s54, s30, 0x100
	v_mov_b32_e32 v27, v26
	v_mov_b64_e32 v[32:33], v[28:29]
	v_mov_b64_e32 v[36:37], v[28:29]
	v_mov_b64_e32 v[48:49], v[28:29]
	v_mov_b64_e32 v[52:53], v[28:29]
	v_mov_b64_e32 v[64:65], v[28:29]
	v_mov_b64_e32 v[68:69], v[28:29]
	v_mov_b64_e32 v[80:81], v[28:29]
	v_mov_b64_e32 v[84:85], v[28:29]
	v_mov_b64_e32 v[40:41], v[28:29]
	v_mov_b64_e32 v[44:45], v[28:29]
	v_mov_b64_e32 v[56:57], v[28:29]
	v_mov_b64_e32 v[60:61], v[28:29]
	v_mov_b64_e32 v[72:73], v[28:29]
	v_mov_b64_e32 v[76:77], v[28:29]
	v_mov_b64_e32 v[88:89], v[28:29]
	v_mov_b64_e32 v[92:93], v[28:29]
	v_mov_b64_e32 v[96:97], v[28:29]
	v_mov_b64_e32 v[100:101], v[28:29]
	v_mov_b64_e32 v[112:113], v[28:29]
	v_mov_b64_e32 v[116:117], v[28:29]
	v_mov_b64_e32 v[128:129], v[28:29]
	v_mov_b64_e32 v[132:133], v[28:29]
	v_mov_b64_e32 v[144:145], v[28:29]
	v_mov_b64_e32 v[148:149], v[28:29]
	v_mov_b64_e32 v[104:105], v[28:29]
	v_mov_b64_e32 v[108:109], v[28:29]
	v_mov_b64_e32 v[120:121], v[28:29]
	v_mov_b64_e32 v[124:125], v[28:29]
	v_mov_b64_e32 v[136:137], v[28:29]
	v_mov_b64_e32 v[140:141], v[28:29]
	v_mov_b64_e32 v[152:153], v[28:29]
	v_mov_b64_e32 v[156:157], v[28:29]
	v_ashrrev_i32_e32 v201, 31, v200
	v_lshl_add_u64 v[204:205], v[202:203], 1, v[2:3]
	v_lshl_add_u64 v[206:207], s[28:29], 0, v[190:191]
	v_lshl_add_u64 v[208:209], s[28:29], 0, v[192:193]
	s_addc_u32 s55, s31, 0
	s_mov_b32 s57, -2
	s_mov_b64 s[30:31], 0
	v_mov_b64_e32 v[30:31], v[26:27]
	v_mov_b64_e32 v[34:35], v[26:27]
	v_mov_b64_e32 v[46:47], v[26:27]
	v_mov_b64_e32 v[50:51], v[26:27]
	v_mov_b64_e32 v[62:63], v[26:27]
	v_mov_b64_e32 v[66:67], v[26:27]
	v_mov_b64_e32 v[78:79], v[26:27]
	v_mov_b64_e32 v[82:83], v[26:27]
	v_mov_b64_e32 v[38:39], v[26:27]
	v_mov_b64_e32 v[42:43], v[26:27]
	v_mov_b64_e32 v[54:55], v[26:27]
	v_mov_b64_e32 v[58:59], v[26:27]
	v_mov_b64_e32 v[70:71], v[26:27]
	v_mov_b64_e32 v[74:75], v[26:27]
	v_mov_b64_e32 v[86:87], v[26:27]
	v_mov_b64_e32 v[90:91], v[26:27]
	v_mov_b64_e32 v[94:95], v[26:27]
	v_mov_b64_e32 v[98:99], v[26:27]
	v_mov_b64_e32 v[110:111], v[26:27]
	v_mov_b64_e32 v[114:115], v[26:27]
	v_mov_b64_e32 v[126:127], v[26:27]
	v_mov_b64_e32 v[130:131], v[26:27]
	v_mov_b64_e32 v[142:143], v[26:27]
	v_mov_b64_e32 v[146:147], v[26:27]
	v_mov_b64_e32 v[102:103], v[26:27]
	v_mov_b64_e32 v[106:107], v[26:27]
	v_mov_b64_e32 v[118:119], v[26:27]
	v_mov_b64_e32 v[122:123], v[26:27]
	v_mov_b64_e32 v[134:135], v[26:27]
	v_mov_b64_e32 v[138:139], v[26:27]
	v_mov_b64_e32 v[150:151], v[26:27]
	v_mov_b64_e32 v[154:155], v[26:27]
	s_branch .LBB0_1709
	.p2align	8

;     ...
;         const bool has_next = S.next(ui + 1, nxt);
;         const char* nA = has_next ? (const char*)g.A + (size_t)nxt.pm * tstepA : cA; const char* nB = has_next ? (const char*)g.Bt + (size_t)nxt.pn * tstepB : cB;
;         for (int t = 0; t < nt; t += 2) {
;             const bool last = (t == nt - 2);
;             const char* a1 = cA + (size_t)(t + 1) * kstep;
;             const char* a2 = last ? nA : cA + (size_t)(t + 2) * kstep; const char* b2 = last ? nB : cB + (size_t)(t + 2) * kstep;
;             const char* a3 = a2 + kstep; const char* b3 = b2 + kstep;
;     ...
;         for (int a = 0; a < 2; ++a)
; #pragma unroll
;             for (int b = 0; b < 2; ++b)
; #pragma unroll
;                 for (int m = 0; m < 4; ++m)
; #pragma unroll
;                     for (int n = 0; n < 2; ++n) acc[a][b][m][n] = (f32x4){0.f, 0.f, 0.f, 0.f};
.LBB0_2081:
	s_ashr_i32 s25, s24, 31
	s_lshl_b64 s[26:27], s[24:25], 20
	s_add_u32 s26, s6, s26
	s_addc_u32 s27, s7, s27
	s_and_b64 s[28:29], s[2:3], exec
	s_cselect_b32 s25, s27, s35
	s_cselect_b32 s58, s26, s34
	s_ashr_i32 s23, s22, 31
	s_lshl_b64 s[28:29], s[22:23], 20
	v_readlane_b32 s38, v249, 42
	v_readlane_b32 s39, v249, 43
	s_add_u32 s28, s38, s28
	s_addc_u32 s29, s39, s29
	s_and_b64 s[38:39], s[2:3], exec
	s_cselect_b32 s23, s29, s37
	s_cselect_b32 s59, s28, s36
	s_add_u32 s60, s36, 0x100
	v_mov_b32_e32 v34, 0
	s_addc_u32 s61, s37, 0
	s_mov_b32 s62, -2
	v_mov_b32_e32 v35, v34
	v_mov_b32_e32 v36, v34
	v_mov_b32_e32 v37, v34
	v_mov_b32_e32 v38, v34
	v_mov_b32_e32 v39, v34
	v_mov_b32_e32 v40, v34
	v_mov_b32_e32 v41, v34
	v_mov_b32_e32 v46, v34
	v_mov_b32_e32 v47, v34
	v_mov_b32_e32 v48, v34
	v_mov_b32_e32 v49, v34
	v_mov_b32_e32 v50, v34
	v_mov_b32_e32 v51, v34
	v_mov_b32_e32 v52, v34
	v_mov_b32_e32 v53, v34
	v_mov_b32_e32 v66, v34
	v_mov_b32_e32 v67, v34
	v_mov_b32_e32 v68, v34
	v_mov_b32_e32 v69, v34
	v_mov_b32_e32 v70, v34
	v_mov_b32_e32 v71, v34
	v_mov_b32_e32 v72, v34
	v_mov_b32_e32 v73, v34
	v_mov_b32_e32 v82, v34
	v_mov_b32_e32 v83, v34
	v_mov_b32_e32 v84, v34
	v_mov_b32_e32 v85, v34
	v_mov_b32_e32 v86, v34
	v_mov_b32_e32 v87, v34
	v_mov_b32_e32 v88, v34
	v_mov_b32_e32 v89, v34
	v_mov_b32_e32 v42, v34
	v_mov_b32_e32 v43, v34
	v_mov_b32_e32 v44, v34
	v_mov_b32_e32 v45, v34
	v_mov_b32_e32 v54, v34
	v_mov_b32_e32 v55, v34
	v_mov_b32_e32 v56, v34
	v_mov_b32_e32 v57, v34
	v_mov_b32_e32 v58, v34
	v_mov_b32_e32 v59, v34
	v_mov_b32_e32 v60, v34
	v_mov_b32_e32 v61, v34
	v_mov_b32_e32 v62, v34
	v_mov_b32_e32 v63, v34
	v_mov_b32_e32 v64, v34
	v_mov_b32_e32 v65, v34
	v_mov_b32_e32 v74, v34
	v_mov_b32_e32 v75, v34
	v_mov_b32_e32 v76, v34
	v_mov_b32_e32 v77, v34
	v_mov_b32_e32 v78, v34
	v_mov_b32_e32 v79, v34
	v_mov_b32_e32 v80, v34
	v_mov_b32_e32 v81, v34
	v_mov_b32_e32 v90, v34
	v_mov_b32_e32 v91, v34
	v_mov_b32_e32 v92, v34
	v_mov_b32_e32 v93, v34
	v_mov_b32_e32 v94, v34
	v_mov_b32_e32 v95, v34
	v_mov_b32_e32 v96, v34
	v_mov_b32_e32 v97, v34
	v_mov_b32_e32 v98, v34
	v_mov_b32_e32 v99, v34
	v_mov_b32_e32 v100, v34
	v_mov_b32_e32 v101, v34
	v_mov_b32_e32 v102, v34
	v_mov_b32_e32 v103, v34
	v_mov_b32_e32 v104, v34
	v_mov_b32_e32 v105, v34
	v_mov_b32_e32 v114, v34
	v_mov_b32_e32 v115, v34
	v_mov_b32_e32 v116, v34
	v_mov_b32_e32 v117, v34
	v_mov_b32_e32 v118, v34
	v_mov_b32_e32 v119, v34
	v_mov_b32_e32 v120, v34
	v_mov_b32_e32 v121, v34
	v_mov_b32_e32 v130, v34
	v_mov_b32_e32 v131, v34
	v_mov_b32_e32 v132, v34
	v_mov_b32_e32 v133, v34
	v_mov_b32_e32 v134, v34
	v_mov_b32_e32 v135, v34
	v_mov_b32_e32 v136, v34
	v_mov_b32_e32 v137, v34
	v_mov_b32_e32 v146, v34
	v_mov_b32_e32 v147, v34
	v_mov_b32_e32 v148, v34
	v_mov_b32_e32 v149, v34
	v_mov_b32_e32 v150, v34
	v_mov_b32_e32 v151, v34
	v_mov_b32_e32 v152, v34
	v_mov_b32_e32 v153, v34
	v_mov_b32_e32 v106, v34
	v_mov_b32_e32 v107, v34
	v_mov_b32_e32 v108, v34
	v_mov_b32_e32 v109, v34
	v_mov_b32_e32 v110, v34
	v_mov_b32_e32 v111, v34
	v_mov_b32_e32 v112, v34
	v_mov_b32_e32 v113, v34
	v_mov_b32_e32 v122, v34
	v_mov_b32_e32 v123, v34
	v_mov_b32_e32 v124, v34
	v_mov_b32_e32 v125, v34
	v_mov_b32_e32 v126, v34
	v_mov_b32_e32 v127, v34
	v_mov_b32_e32 v128, v34
	v_mov_b32_e32 v129, v34
	v_mov_b32_e32 v138, v34
	v_mov_b32_e32 v139, v34
	v_mov_b32_e32 v140, v34
	v_mov_b32_e32 v141, v34
	v_mov_b32_e32 v142, v34
	v_mov_b32_e32 v143, v34
	v_mov_b32_e32 v144, v34
	v_mov_b32_e32 v145, v34
	v_mov_b32_e32 v154, v34
	v_mov_b32_e32 v155, v34
	v_mov_b32_e32 v156, v34
	v_mov_b32_e32 v157, v34
	v_mov_b32_e32 v158, v34
	v_mov_b32_e32 v159, v34
	v_mov_b32_e32 v160, v34
	v_mov_b32_e32 v161, v34
	.p2align	8

;     ...
;         const bool has_next = S.next(ui + 1, nxt);
;         const char* nA = has_next ? (const char*)g.A + (size_t)nxt.pm * tstepA : cA; const char* nB = has_next ? (const char*)g.Bt + (size_t)nxt.pn * tstepB : cB;
;         for (int t = 0; t < nt; t += 2) {
;             const bool last = (t == nt - 2);
;             const char* a1 = cA + (size_t)(t + 1) * kstep;
;             const char* a2 = last ? nA : cA + (size_t)(t + 2) * kstep; const char* b2 = last ? nB : cB + (size_t)(t + 2) * kstep;
;             const char* a3 = a2 + kstep; const char* b3 = b2 + kstep;
;     ...
;         for (int a = 0; a < 2; ++a)
; #pragma unroll
;             for (int b = 0; b < 2; ++b)
; #pragma unroll
;                 for (int m = 0; m < 4; ++m)
; #pragma unroll
;                     for (int n = 0; n < 2; ++n) acc[a][b][m][n] = (f32x4){0.f, 0.f, 0.f, 0.f};
.LBB0_2357:
	s_ashr_i32 s17, s16, 31
	s_lshl_b64 s[18:19], s[16:17], 20
	v_readlane_b32 s20, v248, 8
	v_readlane_b32 s21, v248, 9
	s_add_u32 s18, s20, s18
	s_addc_u32 s19, s21, s19
	s_and_b64 s[20:21], s[2:3], exec
	s_cselect_b32 s17, s19, s25
	s_cselect_b32 s48, s18, s24
	s_ashr_i32 s15, s14, 31
	s_lshl_b64 s[20:21], s[14:15], 20
	v_readlane_b32 s28, v249, 52
	v_readlane_b32 s29, v249, 53
	s_add_u32 s20, s28, s20
	s_addc_u32 s21, s29, s21
	s_and_b64 s[28:29], s[2:3], exec
	s_cselect_b32 s15, s21, s27
	s_cselect_b32 s49, s20, s26
	s_add_u32 s50, s26, 0x100
	v_mov_b32_e32 v34, 0
	s_addc_u32 s51, s27, 0
	s_mov_b32 s52, -2
	v_mov_b32_e32 v35, v34
	v_mov_b32_e32 v36, v34
	v_mov_b32_e32 v37, v34
	v_mov_b32_e32 v38, v34
	v_mov_b32_e32 v39, v34
	v_mov_b32_e32 v40, v34
	v_mov_b32_e32 v41, v34
	v_mov_b32_e32 v46, v34
	v_mov_b32_e32 v47, v34
	v_mov_b32_e32 v48, v34
	v_mov_b32_e32 v49, v34
	v_mov_b32_e32 v54, v34
	v_mov_b32_e32 v55, v34
	v_mov_b32_e32 v56, v34
	v_mov_b32_e32 v57, v34
	v_mov_b32_e32 v62, v34
	v_mov_b32_e32 v63, v34
	v_mov_b32_e32 v64, v34
	v_mov_b32_e32 v65, v34
	v_mov_b32_e32 v70, v34
	v_mov_b32_e32 v71, v34
	v_mov_b32_e32 v72, v34
	v_mov_b32_e32 v73, v34
	v_mov_b32_e32 v78, v34
	v_mov_b32_e32 v79, v34
	v_mov_b32_e32 v80, v34
	v_mov_b32_e32 v81, v34
	v_mov_b32_e32 v86, v34
	v_mov_b32_e32 v87, v34
	v_mov_b32_e32 v88, v34
	v_mov_b32_e32 v89, v34
	v_mov_b32_e32 v42, v34
	v_mov_b32_e32 v43, v34
	v_mov_b32_e32 v44, v34
	v_mov_b32_e32 v45, v34
	v_mov_b32_e32 v50, v34
	v_mov_b32_e32 v51, v34
	v_mov_b32_e32 v52, v34
	v_mov_b32_e32 v53, v34
	v_mov_b32_e32 v58, v34
	v_mov_b32_e32 v59, v34
	v_mov_b32_e32 v60, v34
	v_mov_b32_e32 v61, v34
	v_mov_b32_e32 v66, v34
	v_mov_b32_e32 v67, v34
	v_mov_b32_e32 v68, v34
	v_mov_b32_e32 v69, v34
	v_mov_b32_e32 v74, v34
	v_mov_b32_e32 v75, v34
	v_mov_b32_e32 v76, v34
	v_mov_b32_e32 v77, v34
	v_mov_b32_e32 v82, v34
	v_mov_b32_e32 v83, v34
	v_mov_b32_e32 v84, v34
	v_mov_b32_e32 v85, v34
	v_mov_b32_e32 v90, v34
	v_mov_b32_e32 v91, v34
	v_mov_b32_e32 v92, v34
	v_mov_b32_e32 v93, v34
	v_mov_b32_e32 v94, v34
	v_mov_b32_e32 v95, v34
	v_mov_b32_e32 v96, v34
	v_mov_b32_e32 v97, v34
	v_mov_b32_e32 v98, v34
	v_mov_b32_e32 v99, v34
	v_mov_b32_e32 v100, v34
	v_mov_b32_e32 v101, v34
	v_mov_b32_e32 v102, v34
	v_mov_b32_e32 v103, v34
	v_mov_b32_e32 v104, v34
	v_mov_b32_e32 v105, v34
	v_mov_b32_e32 v110, v34
	v_mov_b32_e32 v111, v34
	v_mov_b32_e32 v112, v34
	v_mov_b32_e32 v113, v34
	v_mov_b32_e32 v118, v34
	v_mov_b32_e32 v119, v34
	v_mov_b32_e32 v120, v34
	v_mov_b32_e32 v121, v34
	v_mov_b32_e32 v126, v34
	v_mov_b32_e32 v127, v34
	v_mov_b32_e32 v128, v34
	v_mov_b32_e32 v129, v34
	v_mov_b32_e32 v134, v34
	v_mov_b32_e32 v135, v34
	v_mov_b32_e32 v136, v34
	v_mov_b32_e32 v137, v34
	v_mov_b32_e32 v142, v34
	v_mov_b32_e32 v143, v34
	v_mov_b32_e32 v144, v34
	v_mov_b32_e32 v145, v34
	v_mov_b32_e32 v150, v34
	v_mov_b32_e32 v151, v34
	v_mov_b32_e32 v152, v34
	v_mov_b32_e32 v153, v34
	v_mov_b32_e32 v106, v34
	v_mov_b32_e32 v107, v34
	v_mov_b32_e32 v108, v34
	v_mov_b32_e32 v109, v34
	v_mov_b32_e32 v114, v34
	v_mov_b32_e32 v115, v34
	v_mov_b32_e32 v116, v34
	v_mov_b32_e32 v117, v34
	v_mov_b32_e32 v122, v34
	v_mov_b32_e32 v123, v34
	v_mov_b32_e32 v124, v34
	v_mov_b32_e32 v125, v34
	v_mov_b32_e32 v130, v34
	v_mov_b32_e32 v131, v34
	v_mov_b32_e32 v132, v34
	v_mov_b32_e32 v133, v34
	v_mov_b32_e32 v138, v34
	v_mov_b32_e32 v139, v34
	v_mov_b32_e32 v140, v34
	v_mov_b32_e32 v141, v34
	v_mov_b32_e32 v146, v34
	v_mov_b32_e32 v147, v34
	v_mov_b32_e32 v148, v34
	v_mov_b32_e32 v149, v34
	v_mov_b32_e32 v154, v34
	v_mov_b32_e32 v155, v34
	v_mov_b32_e32 v156, v34
	v_mov_b32_e32 v157, v34
	v_mov_b32_e32 v158, v34
	v_mov_b32_e32 v159, v34
	v_mov_b32_e32 v160, v34
	v_mov_b32_e32 v161, v34
	.p2align	8

;     ...
;         const bool has_next = S.next(ui + 1, nxt);
;         const char* nA = has_next ? (const char*)g.A + (size_t)nxt.pm * tstepA : cA; const char* nB = has_next ? (const char*)g.Bt + (size_t)nxt.pn * tstepB : cB;
;         for (int t = 0; t < nt; t += 2) {
;             const bool last = (t == nt - 2);
;             const char* a1 = cA + (size_t)(t + 1) * kstep;
;             const char* a2 = last ? nA : cA + (size_t)(t + 2) * kstep; const char* b2 = last ? nB : cB + (size_t)(t + 2) * kstep;
;             const char* a3 = a2 + kstep; const char* b3 = b2 + kstep;
;     ...
;         for (int a = 0; a < 2; ++a)
; #pragma unroll
;             for (int b = 0; b < 2; ++b)
; #pragma unroll
;                 for (int m = 0; m < 4; ++m)
; #pragma unroll
;                     for (int n = 0; n < 2; ++n) acc[a][b][m][n] = (f32x4){0.f, 0.f, 0.f, 0.f};
.LBB0_2647:
	s_add_u32 s81, s46, 0x100
	v_mov_b32_e32 v32, 0
	s_addc_u32 s82, s47, 0
	s_mov_b32 s83, -2
	v_mov_b32_e32 v33, v32
	v_mov_b32_e32 v34, v32
	v_mov_b32_e32 v35, v32
	v_mov_b32_e32 v36, v32
	v_mov_b32_e32 v37, v32
	v_mov_b32_e32 v38, v32
	v_mov_b32_e32 v39, v32
	v_mov_b32_e32 v40, v32
	v_mov_b32_e32 v41, v32
	v_mov_b32_e32 v42, v32
	v_mov_b32_e32 v43, v32
	v_mov_b32_e32 v48, v32
	v_mov_b32_e32 v49, v32
	v_mov_b32_e32 v50, v32
	v_mov_b32_e32 v51, v32
	v_mov_b32_e32 v64, v32
	v_mov_b32_e32 v65, v32
	v_mov_b32_e32 v66, v32
	v_mov_b32_e32 v67, v32
	v_mov_b32_e32 v68, v32
	v_mov_b32_e32 v69, v32
	v_mov_b32_e32 v70, v32
	v_mov_b32_e32 v71, v32
	v_mov_b32_e32 v80, v32
	v_mov_b32_e32 v81, v32
	v_mov_b32_e32 v82, v32
	v_mov_b32_e32 v83, v32
	v_mov_b32_e32 v84, v32
	v_mov_b32_e32 v85, v32
	v_mov_b32_e32 v86, v32
	v_mov_b32_e32 v87, v32
	v_mov_b32_e32 v44, v32
	v_mov_b32_e32 v45, v32
	v_mov_b32_e32 v46, v32
	v_mov_b32_e32 v47, v32
	v_mov_b32_e32 v52, v32
	v_mov_b32_e32 v53, v32
	v_mov_b32_e32 v54, v32
	v_mov_b32_e32 v55, v32
	v_mov_b32_e32 v56, v32
	v_mov_b32_e32 v57, v32
	v_mov_b32_e32 v58, v32
	v_mov_b32_e32 v59, v32
	v_mov_b32_e32 v60, v32
	v_mov_b32_e32 v61, v32
	v_mov_b32_e32 v62, v32
	v_mov_b32_e32 v63, v32
	v_mov_b32_e32 v72, v32
	v_mov_b32_e32 v73, v32
	v_mov_b32_e32 v74, v32
	v_mov_b32_e32 v75, v32
	v_mov_b32_e32 v76, v32
	v_mov_b32_e32 v77, v32
	v_mov_b32_e32 v78, v32
	v_mov_b32_e32 v79, v32
	v_mov_b32_e32 v88, v32
	v_mov_b32_e32 v89, v32
	v_mov_b32_e32 v90, v32
	v_mov_b32_e32 v91, v32
	v_mov_b32_e32 v92, v32
	v_mov_b32_e32 v93, v32
	v_mov_b32_e32 v94, v32
	v_mov_b32_e32 v95, v32
	v_mov_b32_e32 v96, v32
	v_mov_b32_e32 v97, v32
	v_mov_b32_e32 v98, v32
	v_mov_b32_e32 v99, v32
	v_mov_b32_e32 v100, v32
	v_mov_b32_e32 v101, v32
	v_mov_b32_e32 v102, v32
	v_mov_b32_e32 v103, v32
	v_mov_b32_e32 v112, v32
	v_mov_b32_e32 v113, v32
	v_mov_b32_e32 v114, v32
	v_mov_b32_e32 v115, v32
	v_mov_b32_e32 v116, v32
	v_mov_b32_e32 v117, v32
	v_mov_b32_e32 v118, v32
	v_mov_b32_e32 v119, v32
	v_mov_b32_e32 v128, v32
	v_mov_b32_e32 v129, v32
	v_mov_b32_e32 v130, v32
	v_mov_b32_e32 v131, v32
	v_mov_b32_e32 v132, v32
	v_mov_b32_e32 v133, v32
	v_mov_b32_e32 v134, v32
	v_mov_b32_e32 v135, v32
	v_mov_b32_e32 v144, v32
	v_mov_b32_e32 v145, v32
	v_mov_b32_e32 v146, v32
	v_mov_b32_e32 v147, v32
	v_mov_b32_e32 v148, v32
	v_mov_b32_e32 v149, v32
	v_mov_b32_e32 v150, v32
	v_mov_b32_e32 v151, v32
	v_mov_b32_e32 v104, v32
	v_mov_b32_e32 v105, v32
	v_mov_b32_e32 v106, v32
	v_mov_b32_e32 v107, v32
	v_mov_b32_e32 v108, v32
	v_mov_b32_e32 v109, v32
	v_mov_b32_e32 v110, v32
	v_mov_b32_e32 v111, v32
	v_mov_b32_e32 v120, v32
	v_mov_b32_e32 v121, v32
	v_mov_b32_e32 v122, v32
	v_mov_b32_e32 v123, v32
	v_mov_b32_e32 v124, v32
	v_mov_b32_e32 v125, v32
	v_mov_b32_e32 v126, v32
	v_mov_b32_e32 v127, v32
	v_mov_b32_e32 v136, v32
	v_mov_b32_e32 v137, v32
	v_mov_b32_e32 v138, v32
	v_mov_b32_e32 v139, v32
	v_mov_b32_e32 v140, v32
	v_mov_b32_e32 v141, v32
	v_mov_b32_e32 v142, v32
	v_mov_b32_e32 v143, v32
	v_mov_b32_e32 v152, v32
	v_mov_b32_e32 v153, v32
	v_mov_b32_e32 v154, v32
	v_mov_b32_e32 v155, v32
	v_mov_b32_e32 v156, v32
	v_mov_b32_e32 v157, v32
	v_mov_b32_e32 v158, v32
	v_mov_b32_e32 v159, v32
	.p2align	8
